# global attention loop: unconditional KV prefetch, K LDS writes hoisted into PV + one barrier per tile, conflict-free K swizzle (row&15)
# speedup vs baseline: 1.0182x; 1.0182x over previous
.LBB0_584:
	v_mov_b32_e32 v0, v193
	v_readlane_b32 s0, v254, 6
	v_mbcnt_lo_u32_b32 v0, -1, v0
	v_mbcnt_hi_u32_b32 v0, -1, v0
	v_add_u32_e32 v203, s0, v0
	s_mul_hi_i32 s0, s19, 0x2aaaaaab
	s_lshr_b32 s1, s0, 31
	s_add_i32 s0, s0, s1
	s_mul_i32 s1, s0, 6
	v_cndmask_b32_e64 v0, 0, 1, s[4:5]
	s_sub_i32 s2, s19, s1
	s_lshl_b32 s10, s0, 8
	v_readfirstlane_b32 s1, v0
	s_and_b32 s24, s1, 1
	s_ashr_i32 s11, s10, 31
	s_mul_i32 s0, s0, 0x240000
	s_mul_hi_i32 s1, s10, 0x2400
	s_add_u32 s3, s34, s0
	s_addc_u32 s6, s35, s1
	s_lshl_b32 s0, s2, 7
	s_ashr_i32 s1, s0, 31
	s_lshl_b64 s[0:1], s[0:1], 1
	s_add_u32 s3, s3, s0
	s_addc_u32 s6, s6, s1
	s_add_u32 s22, s3, 0x1200
	s_mulk_i32 s2, 0x56
	s_addc_u32 s23, s6, 0
	s_bfe_u32 s3, s2, 0x1000f
	s_bfe_u32 s2, s2, 0x80008
	s_add_i32 s2, s2, s3
	s_sext_i32_i8 s2, s2
	s_lshl_b32 s2, s2, 7
	s_ashr_i32 s3, s2, 31
	s_lshl_b64 s[2:3], s[2:3], 1
	s_add_u32 s6, s15, s2
	s_addc_u32 s7, s16, s3
	s_add_u32 s8, s17, s2
	s_addc_u32 s9, s18, s3
	s_lshl_b64 s[10:11], s[10:11], 12
	v_readlane_b32 s20, v254, 42
	v_ashrrev_i32_e32 v0, 1, v203
	s_add_u32 s20, s20, s10
	v_readlane_b32 s10, v254, 44
	v_bfe_u32 v201, v203, 5, 1
	v_and_b32_e32 v182, 0xffffffe0, v0
	v_bfi_b32 v2, s67, v0, v203
	v_mov_b64_e32 v[0:1], s[22:23]
	s_addc_u32 s21, s10, s11
	v_mad_i64_i32 v[0:1], s[10:11], v2, s66, v[0:1]
	v_lshlrev_b32_e32 v184, 4, v201
	v_mov_b32_e32 v185, v193
	v_lshl_add_u64 v[150:151], v[0:1], 0, v[184:185]
	v_ashrrev_i32_e32 v0, 4, v203
	v_add_u32_e32 v7, 32, v0
	v_and_b32_e32 v3, 0xfffff0, v0
	v_lshlrev_b32_e32 v4, 1, v0
	v_and_b32_e32 v8, 0xfffff0, v7
	v_lshlrev_b32_e32 v9, 1, v7
	v_lshlrev_b32_e32 v1, 3, v203
	v_and_or_b32 v3, v4, 8, v3
	v_and_or_b32 v8, v9, 8, v8
	v_and_b32_e32 v2, 0x78, v1
	v_lshrrev_b32_e32 v4, 1, v0
	v_lshrrev_b32_e32 v3, 1, v3
	v_bfe_u32 v1, v1, 5, 2
	v_and_b32_e32 v5, 3, v0
	v_lshrrev_b32_e32 v8, 1, v8
	v_or_b32_e32 v3, v3, v1
	v_and_or_b32 v4, v4, 4, v5
	v_lshlrev_b32_e32 v5, 1, v2
	v_or_b32_e32 v1, v8, v1
	v_lshlrev_b32_e32 v3, 9, v3
	v_lshlrev_b32_e32 v4, 6, v4
	v_and_b32_e32 v6, 48, v5
	v_lshlrev_b32_e32 v1, 9, v1
	v_and_b32_e32 v202, 63, v203
	v_or3_b32 v3, v3, v4, v6
	v_or3_b32 v1, v1, v4, v6
	v_lshlrev_b32_e32 v6, 4, v203
	v_lshlrev_b32_e32 v4, 3, v202
	v_and_b32_e32 v6, 0xc0, v6
	v_lshlrev_b32_e32 v8, 1, v203
	v_and_or_b32 v6, v4, 24, v6
	v_and_b32_e32 v8, 32, v8
	v_and_b32_e32 v4, 0x100, v4
	v_or3_b32 v174, v6, v8, v4
	v_mul_lo_u32 v4, v0, s68
	v_or_b32_e32 v2, v4, v2
	s_cmp_lg_u32 0, -1
	v_and_b32_e32 v200, 31, v203
	v_lshlrev_b32_e32 v192, 1, v2
	v_lshlrev_b32_e32 v2, 8, v0
	v_and_b32_e32 v4, 0xf0, v203
	v_lshlrev_b32_e32 v6, 8, v7
	s_cselect_b32 s25, 0, 0
	v_add_u32_e32 v148, 0x48000, v192
	v_mov_b32_e32 v149, v193
	v_bitop3_b32 v2, v5, v2, v4 bitop3:0xde
	v_bitop3_b32 v4, v5, v6, v4 bitop3:0xde
	v_lshlrev_b32_e32 v5, 4, v200
	v_mul_lo_u32 v0, v0, s66
	v_and_b32_e32 v6, 15, v203
	s_cmp_eq_u32 s24, 0
	v_add_u32_e32 v185, s25, v174
	v_lshl_add_u64 v[152:153], s[8:9], 0, v[192:193]
	v_lshl_add_u64 v[154:155], s[8:9], 0, v[148:149]
	v_lshl_add_u64 v[156:157], s[6:7], 0, v[192:193]
	v_lshl_add_u64 v[158:159], s[6:7], 0, v[148:149]
	s_mov_b64 s[10:11], -1
	v_lshlrev_b32_e32 v175, 8, v200
	v_add_u32_e32 v204, 0, v3
	v_add_u32_e32 v205, 0, v1
	v_add_u32_e32 v206, 0, v2
	v_add_u32_e32 v207, 0, v4
	v_and_b32_e32 v188, 0xf0, v5
	v_or_b32_e32 v211, 32, v184
	v_or_b32_e32 v210, 64, v184
	v_or_b32_e32 v209, 0x60, v184
	v_or_b32_e32 v208, 0x80, v184
	v_or_b32_e32 v191, 0xa0, v184
	v_or_b32_e32 v190, 0xc0, v184
	v_or_b32_e32 v189, 0xe0, v184
	v_lshl_or_b32 v186, v6, 4, v0
	s_cbranch_scc1 .LBB0_586
	s_and_b64 vcc, exec, s[10:11]
	s_cbranch_vccz .LBB0_583
	s_branch .LBB0_591

.LBB0_592:
	v_add_f32_e32 v188, v234, v235
	v_add_f32_e32 v183, v183, v188
	v_add_f32_e32 v188, v222, v223
	s_add_i32 s8, s8, 2
	v_add_f32_e32 v183, v183, v188
	ds_read_b64_tr_b16 v[188:189], v177 offset:0
	ds_read_b64_tr_b16 v[190:191], v177 offset:0x800
	ds_read_b64_tr_b16 v[222:223], v177 offset:0x1000
	ds_read_b64_tr_b16 v[224:225], v177 offset:0x1800
	ds_read_b64_tr_b16 v[226:227], v177 offset:0x2000
	ds_read_b64_tr_b16 v[228:229], v177 offset:0x2800
	ds_read_b64_tr_b16 v[230:231], v177 offset:0x3000
	ds_read_b64_tr_b16 v[232:233], v177 offset:0x3800
	s_waitcnt lgkmcnt(0)
	s_nop 0
	v_mfma_f32_32x32x16_bf16 v[0:15], v[80:83], v[188:191], v[0:15]
	ds_read_b64_tr_b16 v[188:189], v177 offset:0x200
	ds_read_b64_tr_b16 v[190:191], v177 offset:0xa00
	v_mfma_f32_32x32x16_bf16 v[0:15], v[84:87], v[222:225], v[0:15]
	ds_read_b64_tr_b16 v[222:223], v177 offset:0x1200
	ds_read_b64_tr_b16 v[224:225], v177 offset:0x1a00
	v_mfma_f32_32x32x16_bf16 v[0:15], v[88:91], v[226:229], v[0:15]
	ds_read_b64_tr_b16 v[226:227], v177 offset:0x2200
	ds_read_b64_tr_b16 v[228:229], v177 offset:0x2a00
	v_mfma_f32_32x32x16_bf16 v[0:15], v[92:95], v[230:233], v[0:15]
	ds_read_b64_tr_b16 v[230:231], v177 offset:0x3200
	ds_read_b64_tr_b16 v[232:233], v177 offset:0x3a00
	s_waitcnt lgkmcnt(0)
	v_mfma_f32_32x32x16_bf16 v[16:31], v[80:83], v[188:191], v[16:31]
	ds_read_b64_tr_b16 v[188:189], v177 offset:0x400
	ds_read_b64_tr_b16 v[190:191], v177 offset:0xc00
	v_mfma_f32_32x32x16_bf16 v[16:31], v[84:87], v[222:225], v[16:31]
	ds_read_b64_tr_b16 v[222:223], v177 offset:0x1400
	ds_read_b64_tr_b16 v[224:225], v177 offset:0x1c00
	v_mfma_f32_32x32x16_bf16 v[16:31], v[88:91], v[226:229], v[16:31]
	ds_read_b64_tr_b16 v[226:227], v177 offset:0x2400
	ds_read_b64_tr_b16 v[228:229], v177 offset:0x2c00
	v_mfma_f32_32x32x16_bf16 v[16:31], v[92:95], v[230:233], v[16:31]
	ds_read_b64_tr_b16 v[230:231], v177 offset:0x3400
	ds_read_b64_tr_b16 v[232:233], v177 offset:0x3c00
	s_waitcnt lgkmcnt(0)
	v_mfma_f32_32x32x16_bf16 v[32:47], v[80:83], v[188:191], v[32:47]
	ds_read_b64_tr_b16 v[188:189], v177 offset:0x600
	ds_read_b64_tr_b16 v[190:191], v177 offset:0xe00
	s_waitcnt vmcnt(4)
	ds_write_b128 v206, v[164:167] offset:49152
	ds_write_b128 v207, v[168:171] offset:49152
	v_mfma_f32_32x32x16_bf16 v[32:47], v[84:87], v[222:225], v[32:47]
	ds_read_b64_tr_b16 v[222:223], v177 offset:0x1600
	ds_read_b64_tr_b16 v[224:225], v177 offset:0x1e00
	v_mfma_f32_32x32x16_bf16 v[32:47], v[88:91], v[226:229], v[32:47]
	ds_read_b64_tr_b16 v[226:227], v177 offset:0x2600
	ds_read_b64_tr_b16 v[228:229], v177 offset:0x2e00
	v_mfma_f32_32x32x16_bf16 v[32:47], v[92:95], v[230:233], v[32:47]
	ds_read_b64_tr_b16 v[230:231], v177 offset:0x3600
	ds_read_b64_tr_b16 v[232:233], v177 offset:0x3e00
	s_waitcnt lgkmcnt(0)
	v_mfma_f32_32x32x16_bf16 v[48:63], v[80:83], v[188:191], v[48:63]
	v_exp_f32_e32 v188, v108
	v_exp_f32_e32 v191, v109
	v_exp_f32_e32 v189, v110
	v_exp_f32_e32 v190, v111
	s_barrier
	v_mfma_f32_32x32x16_bf16 v[48:63], v[84:87], v[222:225], v[48:63]
	v_exp_f32_e32 v223, v104
	v_exp_f32_e32 v225, v105
	v_exp_f32_e32 v222, v106
	v_exp_f32_e32 v224, v107
	s_waitcnt vmcnt(4)
	s_add_u32 s2, s2, 0x120000
	s_addc_u32 s3, s3, 0
	v_mfma_f32_32x32x16_bf16 v[48:63], v[88:91], v[226:229], v[48:63]
	v_exp_f32_e32 v229, v98
	v_exp_f32_e32 v228, v100
	v_exp_f32_e32 v226, v102
	v_exp_f32_e32 v227, v103
	s_and_b64 vcc, exec, s[6:7]
	ds_write_b128 v204, v[160:163] offset:16384
	ds_write_b128 v205, v[172:175] offset:16384
	v_mfma_f32_32x32x16_bf16 v[48:63], v[92:95], v[230:233], v[48:63]
	v_exp_f32_e32 v231, v96
	v_exp_f32_e32 v233, v97
	v_exp_f32_e32 v232, v99
	v_exp_f32_e32 v230, v101
	s_cbranch_vccnz .Lga_exit
.LBB0_593:
	ds_read_b128 v[80:83], v212 offset:49152
	ds_read_b128 v[84:87], v212 offset:57344
	ds_read_b128 v[160:163], v211 offset:49152
	ds_read_b128 v[164:167], v211 offset:57344
	v_exp_f32_e32 v168, v72
	v_exp_f32_e32 v169, v73
	s_waitcnt lgkmcnt(3)
	v_mfma_f32_32x32x16_bf16 v[96:111], v[80:83], v[140:143], 0
	v_exp_f32_e32 v170, v74
	v_exp_f32_e32 v171, v75
	v_exp_f32_e32 v172, v76
	v_exp_f32_e32 v173, v77
	v_exp_f32_e32 v174, v78
	v_exp_f32_e32 v79, v79
	s_waitcnt lgkmcnt(2)
	v_mfma_f32_32x32x16_bf16 v[80:95], v[84:87], v[140:143], 0
	s_waitcnt lgkmcnt(1)
	v_mfma_f32_32x32x16_bf16 v[96:111], v[160:163], v[136:139], v[96:111]
	s_waitcnt lgkmcnt(0)
	v_mfma_f32_32x32x16_bf16 v[80:95], v[164:167], v[136:139], v[80:95]
	ds_read_b128 v[160:163], v210 offset:49152
	ds_read_b128 v[164:167], v210 offset:57344
	s_waitcnt lgkmcnt(1)
	v_mfma_f32_32x32x16_bf16 v[96:111], v[160:163], v[132:135], v[96:111]
	s_waitcnt lgkmcnt(0)
	v_mfma_f32_32x32x16_bf16 v[80:95], v[164:167], v[132:135], v[80:95]
	ds_read_b128 v[160:163], v209 offset:49152
	ds_read_b128 v[164:167], v209 offset:57344
	s_waitcnt lgkmcnt(1)
	v_mfma_f32_32x32x16_bf16 v[96:111], v[160:163], v[128:131], v[96:111]
	s_waitcnt lgkmcnt(0)
	v_mfma_f32_32x32x16_bf16 v[80:95], v[164:167], v[128:131], v[80:95]
	ds_read_b128 v[160:163], v208 offset:49152
	ds_read_b128 v[164:167], v208 offset:57344
	s_waitcnt lgkmcnt(1)
	v_mfma_f32_32x32x16_bf16 v[96:111], v[160:163], v[124:127], v[96:111]
	s_waitcnt lgkmcnt(0)
	v_mfma_f32_32x32x16_bf16 v[80:95], v[164:167], v[124:127], v[80:95]
	ds_read_b128 v[160:163], v213 offset:49152
	ds_read_b128 v[164:167], v213 offset:57344
	s_waitcnt lgkmcnt(1)
	v_mfma_f32_32x32x16_bf16 v[96:111], v[160:163], v[120:123], v[96:111]
	s_waitcnt lgkmcnt(0)
	v_mfma_f32_32x32x16_bf16 v[80:95], v[164:167], v[120:123], v[80:95]
	ds_read_b128 v[160:163], v214 offset:49152
	ds_read_b128 v[164:167], v214 offset:57344
	s_waitcnt lgkmcnt(1)
	v_mfma_f32_32x32x16_bf16 v[96:111], v[160:163], v[116:119], v[96:111]
	s_waitcnt lgkmcnt(0)
	v_mfma_f32_32x32x16_bf16 v[80:95], v[164:167], v[116:119], v[80:95]
	ds_read_b128 v[160:163], v215 offset:49152
	ds_read_b128 v[164:167], v215 offset:57344
	s_waitcnt lgkmcnt(1)
	v_mfma_f32_32x32x16_bf16 v[96:111], v[160:163], v[112:115], v[96:111]
	v_exp_f32_e32 v160, v64
	v_add_f32_e32 v64, 0, v231
	v_add_f32_e32 v64, v233, v64
	v_add_f32_e32 v64, v229, v64
	v_add_f32_e32 v64, v232, v64
	v_add_f32_e32 v64, v228, v64
	v_add_f32_e32 v64, v230, v64
	v_add_f32_e32 v64, v226, v64
	v_add_f32_e32 v64, v227, v64
	v_add_f32_e32 v64, v223, v64
	v_add_f32_e32 v64, v225, v64
	v_add_f32_e32 v64, v222, v64
	v_add_f32_e32 v64, v224, v64
	v_add_f32_e32 v64, v188, v64
	v_exp_f32_e32 v161, v65
	v_add_f32_e32 v64, v191, v64
	v_exp_f32_e32 v162, v66
	v_add_f32_e32 v64, v189, v64
	v_exp_f32_e32 v163, v67
	v_add_f32_e32 v64, v190, v64
	s_waitcnt lgkmcnt(0)
	v_mfma_f32_32x32x16_bf16 v[80:95], v[164:167], v[112:115], v[80:95]
	v_exp_f32_e32 v164, v68
	v_add_f32_e32 v64, v160, v64
	v_exp_f32_e32 v165, v69
	v_add_f32_e32 v64, v161, v64
	v_exp_f32_e32 v166, v70
	v_add_f32_e32 v64, v162, v64
	v_exp_f32_e32 v167, v71
	v_add_f32_e32 v64, v163, v64
	v_add_f32_e32 v64, v164, v64
	v_add_f32_e32 v64, v165, v64
	v_add_f32_e32 v64, v166, v64
	v_add_f32_e32 v64, v167, v64
	v_add_f32_e32 v64, v168, v64
	v_add_f32_e32 v64, v169, v64
	v_add_f32_e32 v64, v170, v64
	v_add_f32_e32 v64, v171, v64
	v_add_f32_e32 v64, v172, v64
	v_add_f32_e32 v64, v173, v64
	v_add_f32_e32 v64, v174, v64
	v_add_f32_e32 v234, v79, v64
	v_mov_b32_e32 v235, v234
	v_cvt_pk_bf16_f32 v64, v231, v233
	v_cvt_pk_bf16_f32 v65, v229, v232
	v_cvt_pk_bf16_f32 v66, v228, v230
	v_cvt_pk_bf16_f32 v67, v226, v227
	v_cvt_pk_bf16_f32 v68, v223, v225
	v_cvt_pk_bf16_f32 v69, v222, v224
	v_cvt_pk_bf16_f32 v70, v188, v191
	v_cvt_pk_bf16_f32 v71, v189, v190
	v_cvt_pk_bf16_f32 v72, v160, v161
	v_cvt_pk_bf16_f32 v73, v162, v163
	v_cvt_pk_bf16_f32 v74, v164, v165
	v_cvt_pk_bf16_f32 v75, v166, v167
	v_cvt_pk_bf16_f32 v76, v168, v169
	v_cvt_pk_bf16_f32 v77, v170, v171
	v_cvt_pk_bf16_f32 v78, v172, v173
	v_cvt_pk_bf16_f32 v79, v174, v79
	s_nop 1
	v_permlane32_swap_b32_e32 v234, v235
	v_permlane32_swap_b32_e32 v64, v66
	v_permlane32_swap_b32_e32 v65, v67
	v_permlane32_swap_b32_e32 v68, v70
	v_permlane32_swap_b32_e32 v69, v71
	v_permlane32_swap_b32_e32 v72, v74
	v_permlane32_swap_b32_e32 v73, v75
	v_permlane32_swap_b32_e32 v76, v78
	v_permlane32_swap_b32_e32 v77, v79
	v_lshl_add_u64 v[190:191], s[2:3], 0, v[186:187]
	s_mov_b32 s6, 0x119b1000
	v_add_co_u32_e32 v164, vcc, s6, v190
	v_lshl_add_u64 v[188:189], s[2:3], 0, v[192:193]
	s_nop 0
	v_addc_co_u32_e32 v165, vcc, 0, v191, vcc
	v_add_co_u32_e32 v168, vcc, s6, v188
	s_nop 1
	v_addc_co_u32_e32 v169, vcc, 0, v189, vcc
	global_load_dwordx4 v[160:163], v[164:165], off offset:2560
	s_nop 0
	global_load_dwordx4 v[164:167], v[164:165], off offset:2048
	s_nop 0
	global_load_dwordx4 v[172:175], v[168:169], off offset:2560
	s_nop 0
	global_load_dwordx4 v[168:171], v[168:169], off offset:2048
	ds_read_b64_tr_b16 v[222:223], v185 offset:0
	ds_read_b64_tr_b16 v[224:225], v185 offset:0x800
	ds_read_b64_tr_b16 v[226:227], v185 offset:0x1000
	ds_read_b64_tr_b16 v[228:229], v185 offset:0x1800
	ds_read_b64_tr_b16 v[230:231], v185 offset:0x2000
	ds_read_b64_tr_b16 v[232:233], v185 offset:0x2800
	ds_read_b64_tr_b16 v[236:237], v185 offset:0x3000
	ds_read_b64_tr_b16 v[238:239], v185 offset:0x3800
	s_waitcnt lgkmcnt(0)
	s_nop 0
	v_mfma_f32_32x32x16_bf16 v[0:15], v[64:67], v[222:225], v[0:15]
	ds_read_b64_tr_b16 v[222:223], v185 offset:0x200
	ds_read_b64_tr_b16 v[224:225], v185 offset:0xa00
	v_mfma_f32_32x32x16_bf16 v[0:15], v[68:71], v[226:229], v[0:15]
	ds_read_b64_tr_b16 v[226:227], v185 offset:0x1200
	ds_read_b64_tr_b16 v[228:229], v185 offset:0x1a00
	v_mfma_f32_32x32x16_bf16 v[0:15], v[72:75], v[230:233], v[0:15]
	ds_read_b64_tr_b16 v[230:231], v185 offset:0x2200
	ds_read_b64_tr_b16 v[232:233], v185 offset:0x2a00
	v_mfma_f32_32x32x16_bf16 v[0:15], v[76:79], v[236:239], v[0:15]
	ds_read_b64_tr_b16 v[236:237], v185 offset:0x3200
	ds_read_b64_tr_b16 v[238:239], v185 offset:0x3a00
	s_waitcnt lgkmcnt(0)
	v_mfma_f32_32x32x16_bf16 v[16:31], v[64:67], v[222:225], v[16:31]
	ds_read_b64_tr_b16 v[222:223], v185 offset:0x400
	ds_read_b64_tr_b16 v[224:225], v185 offset:0xc00
	v_mfma_f32_32x32x16_bf16 v[16:31], v[68:71], v[226:229], v[16:31]
	ds_read_b64_tr_b16 v[226:227], v185 offset:0x1400
	ds_read_b64_tr_b16 v[228:229], v185 offset:0x1c00
	v_mfma_f32_32x32x16_bf16 v[16:31], v[72:75], v[230:233], v[16:31]
	ds_read_b64_tr_b16 v[230:231], v185 offset:0x2400
	ds_read_b64_tr_b16 v[232:233], v185 offset:0x2c00
	v_mfma_f32_32x32x16_bf16 v[16:31], v[76:79], v[236:239], v[16:31]
	ds_read_b64_tr_b16 v[236:237], v185 offset:0x3400
	ds_read_b64_tr_b16 v[238:239], v185 offset:0x3c00
	s_waitcnt lgkmcnt(0)
	v_mfma_f32_32x32x16_bf16 v[32:47], v[64:67], v[222:225], v[32:47]
	ds_read_b64_tr_b16 v[222:223], v185 offset:0x600
	ds_read_b64_tr_b16 v[224:225], v185 offset:0xe00
	s_waitcnt vmcnt(4)
	ds_write_b128 v206, v[148:151] offset:32768
	ds_write_b128 v207, v[156:159] offset:32768
	v_mfma_f32_32x32x16_bf16 v[32:47], v[68:71], v[226:229], v[32:47]
	ds_read_b64_tr_b16 v[226:227], v185 offset:0x1600
	ds_read_b64_tr_b16 v[228:229], v185 offset:0x1e00
	v_mfma_f32_32x32x16_bf16 v[32:47], v[72:75], v[230:233], v[32:47]
	ds_read_b64_tr_b16 v[230:231], v185 offset:0x2600
	ds_read_b64_tr_b16 v[232:233], v185 offset:0x2e00
	v_mfma_f32_32x32x16_bf16 v[32:47], v[76:79], v[236:239], v[32:47]
	ds_read_b64_tr_b16 v[236:237], v185 offset:0x3600
	ds_read_b64_tr_b16 v[238:239], v185 offset:0x3e00
	s_waitcnt lgkmcnt(0)
	v_mfma_f32_32x32x16_bf16 v[48:63], v[64:67], v[222:225], v[48:63]
	s_barrier
	s_waitcnt vmcnt(4)
	v_exp_f32_e32 v218, v96
	v_exp_f32_e32 v219, v97
	v_exp_f32_e32 v220, v98
	v_mfma_f32_32x32x16_bf16 v[48:63], v[68:71], v[226:229], v[48:63]
	v_exp_f32_e32 v221, v99
	v_exp_f32_e32 v240, v108
	v_exp_f32_e32 v241, v109
	v_exp_f32_e32 v242, v110
	v_exp_f32_e32 v243, v111
	s_waitcnt vmcnt(7)
	ds_write_b128 v204, v[144:147]
	s_waitcnt vmcnt(6)
	ds_write_b128 v205, v[152:155]
	v_mfma_f32_32x32x16_bf16 v[48:63], v[72:75], v[230:233], v[48:63]
	v_exp_f32_e32 v230, v100
	v_exp_f32_e32 v231, v101
	v_exp_f32_e32 v232, v102
	v_exp_f32_e32 v233, v103
	v_mfma_f32_32x32x16_bf16 v[48:63], v[76:79], v[236:239], v[48:63]
	v_exp_f32_e32 v236, v104
	v_exp_f32_e32 v237, v105
	v_exp_f32_e32 v238, v106
	v_exp_f32_e32 v239, v107
	ds_read_b128 v[64:67], v212 offset:32768
	ds_read_b128 v[68:71], v212 offset:40960
	ds_read_b128 v[222:225], v211 offset:32768
	ds_read_b128 v[226:229], v211 offset:40960
	v_exp_f32_e32 v244, v86
	v_exp_f32_e32 v245, v87
	s_waitcnt lgkmcnt(3)
	v_mfma_f32_32x32x16_bf16 v[96:111], v[64:67], v[140:143], 0
	v_exp_f32_e32 v246, v88
	v_exp_f32_e32 v247, v89
	v_exp_f32_e32 v248, v90
	v_exp_f32_e32 v249, v91
	v_exp_f32_e32 v250, v92
	v_exp_f32_e32 v251, v93
	v_exp_f32_e32 v252, v94
	s_waitcnt lgkmcnt(2)
	v_mfma_f32_32x32x16_bf16 v[64:79], v[68:71], v[140:143], 0
	v_exp_f32_e32 v95, v95
	s_waitcnt lgkmcnt(1)
	v_mfma_f32_32x32x16_bf16 v[96:111], v[222:225], v[136:139], v[96:111]
	s_waitcnt lgkmcnt(0)
	v_mfma_f32_32x32x16_bf16 v[64:79], v[226:229], v[136:139], v[64:79]
	ds_read_b128 v[222:225], v210 offset:32768
	ds_read_b128 v[226:229], v210 offset:40960
	s_waitcnt lgkmcnt(1)
	v_mfma_f32_32x32x16_bf16 v[96:111], v[222:225], v[132:135], v[96:111]
	s_waitcnt lgkmcnt(0)
	v_mfma_f32_32x32x16_bf16 v[64:79], v[226:229], v[132:135], v[64:79]
	ds_read_b128 v[222:225], v209 offset:32768
	ds_read_b128 v[226:229], v209 offset:40960
	s_waitcnt lgkmcnt(1)
	v_mfma_f32_32x32x16_bf16 v[96:111], v[222:225], v[128:131], v[96:111]
	s_waitcnt lgkmcnt(0)
	v_mfma_f32_32x32x16_bf16 v[64:79], v[226:229], v[128:131], v[64:79]
	ds_read_b128 v[222:225], v208 offset:32768
	ds_read_b128 v[226:229], v208 offset:40960
	s_waitcnt lgkmcnt(1)
	v_mfma_f32_32x32x16_bf16 v[96:111], v[222:225], v[124:127], v[96:111]
	s_waitcnt lgkmcnt(0)
	v_mfma_f32_32x32x16_bf16 v[64:79], v[226:229], v[124:127], v[64:79]
	ds_read_b128 v[222:225], v213 offset:32768
	ds_read_b128 v[226:229], v213 offset:40960
	s_waitcnt lgkmcnt(1)
	v_mfma_f32_32x32x16_bf16 v[96:111], v[222:225], v[120:123], v[96:111]
	s_waitcnt lgkmcnt(0)
	v_mfma_f32_32x32x16_bf16 v[64:79], v[226:229], v[120:123], v[64:79]
	ds_read_b128 v[222:225], v214 offset:32768
	ds_read_b128 v[226:229], v214 offset:40960
	s_waitcnt lgkmcnt(1)
	v_mfma_f32_32x32x16_bf16 v[96:111], v[222:225], v[116:119], v[96:111]
	s_waitcnt lgkmcnt(0)
	v_mfma_f32_32x32x16_bf16 v[64:79], v[226:229], v[116:119], v[64:79]
	ds_read_b128 v[222:225], v215 offset:32768
	ds_read_b128 v[226:229], v215 offset:40960
	s_waitcnt lgkmcnt(1)
	v_mfma_f32_32x32x16_bf16 v[96:111], v[222:225], v[112:115], v[96:111]
	v_exp_f32_e32 v224, v80
	v_add_f32_e32 v80, 0, v218
	v_add_f32_e32 v80, v219, v80
	v_add_f32_e32 v80, v220, v80
	v_add_f32_e32 v80, v221, v80
	v_add_f32_e32 v80, v230, v80
	v_add_f32_e32 v80, v231, v80
	v_add_f32_e32 v80, v232, v80
	v_add_f32_e32 v80, v233, v80
	v_add_f32_e32 v80, v236, v80
	v_add_f32_e32 v80, v237, v80
	v_add_f32_e32 v80, v238, v80
	v_add_f32_e32 v80, v239, v80
	v_add_f32_e32 v80, v240, v80
	v_exp_f32_e32 v225, v81
	v_add_f32_e32 v80, v241, v80
	s_waitcnt lgkmcnt(0)
	v_mfma_f32_32x32x16_bf16 v[64:79], v[226:229], v[112:115], v[64:79]
	v_exp_f32_e32 v226, v82
	v_add_f32_e32 v80, v242, v80
	v_exp_f32_e32 v227, v83
	v_add_f32_e32 v80, v243, v80
	v_exp_f32_e32 v228, v84
	v_add_f32_e32 v80, v224, v80
	v_exp_f32_e32 v229, v85
	v_add_f32_e32 v80, v225, v80
	v_add_f32_e32 v80, v226, v80
	v_add_f32_e32 v80, v227, v80
	v_add_f32_e32 v80, v228, v80
	v_add_f32_e32 v80, v229, v80
	v_add_f32_e32 v80, v244, v80
	v_add_f32_e32 v80, v245, v80
	v_add_f32_e32 v80, v246, v80
	v_add_f32_e32 v80, v247, v80
	v_add_f32_e32 v80, v248, v80
	v_add_f32_e32 v80, v249, v80
	v_add_f32_e32 v80, v250, v80
	v_add_f32_e32 v80, v251, v80
	v_add_f32_e32 v80, v252, v80
	v_add_f32_e32 v222, v95, v80
	v_mov_b32_e32 v223, v222
	v_cvt_pk_bf16_f32 v80, v218, v219
	v_cvt_pk_bf16_f32 v81, v220, v221
	v_cvt_pk_bf16_f32 v82, v230, v231
	v_cvt_pk_bf16_f32 v83, v232, v233
	v_cvt_pk_bf16_f32 v84, v236, v237
	v_cvt_pk_bf16_f32 v85, v238, v239
	v_cvt_pk_bf16_f32 v86, v240, v241
	v_cvt_pk_bf16_f32 v87, v242, v243
	v_cvt_pk_bf16_f32 v88, v224, v225
	v_cvt_pk_bf16_f32 v89, v226, v227
	v_cvt_pk_bf16_f32 v90, v228, v229
	v_cvt_pk_bf16_f32 v91, v244, v245
	v_cvt_pk_bf16_f32 v92, v246, v247
	v_cvt_pk_bf16_f32 v93, v248, v249
	v_cvt_pk_bf16_f32 v94, v250, v251
	v_cvt_pk_bf16_f32 v95, v252, v95
	s_nop 1
	v_permlane32_swap_b32_e32 v222, v223
	v_permlane32_swap_b32_e32 v80, v82
	v_permlane32_swap_b32_e32 v81, v83
	v_permlane32_swap_b32_e32 v84, v86
	v_permlane32_swap_b32_e32 v85, v87
	v_permlane32_swap_b32_e32 v88, v90
	v_permlane32_swap_b32_e32 v89, v91
	v_permlane32_swap_b32_e32 v92, v94
	v_permlane32_swap_b32_e32 v93, v95
	s_cmpk_gt_u32 s8, 0x100
	s_cselect_b64 s[6:7], -1, 0
	v_add_co_u32_e32 v148, vcc, 0x11a41000, v190
	s_nop 1
	v_addc_co_u32_e32 v149, vcc, 0, v191, vcc
	v_add_co_u32_e32 v156, vcc, 0x11a41000, v188
	s_nop 1
	v_addc_co_u32_e32 v157, vcc, 0, v189, vcc
	global_load_dwordx4 v[144:147], v[148:149], off offset:2560
	s_nop 0
	global_load_dwordx4 v[148:151], v[148:149], off offset:2048
	s_nop 0
	global_load_dwordx4 v[152:155], v[156:157], off offset:2560
	s_nop 0
	global_load_dwordx4 v[156:159], v[156:157], off offset:2048
	s_branch .LBB0_592

.LBB0_595:
	s_waitcnt vmcnt(0)
	v_and_b32_e32 v80, 0x3fffffc0, v203
	s_add_i32 s2, 0, 0x10000
	v_lshl_add_u32 v144, v80, 2, s2
	ds_read_b128 v[80:83], v212 offset:49152
	ds_read_b128 v[84:87], v212 offset:57344
	v_exp_f32_e32 v65, v65
	v_exp_f32_e32 v67, v67
	s_waitcnt lgkmcnt(1)
	v_mfma_f32_32x32x16_bf16 v[96:111], v[80:83], v[140:143], 0
	s_waitcnt lgkmcnt(0)
	v_mfma_f32_32x32x16_bf16 v[80:95], v[84:87], v[140:143], 0
	ds_read_b128 v[140:143], v211 offset:49152
	ds_read_b128 v[146:149], v211 offset:57344
	s_waitcnt lgkmcnt(1)
	v_mfma_f32_32x32x16_bf16 v[96:111], v[140:143], v[136:139], v[96:111]
	s_waitcnt lgkmcnt(0)
	v_mfma_f32_32x32x16_bf16 v[80:95], v[146:149], v[136:139], v[80:95]
	ds_read_b128 v[136:139], v210 offset:49152
	ds_read_b128 v[140:143], v210 offset:57344
	s_waitcnt lgkmcnt(1)
	v_mfma_f32_32x32x16_bf16 v[96:111], v[136:139], v[132:135], v[96:111]
	s_waitcnt lgkmcnt(0)
	v_mfma_f32_32x32x16_bf16 v[80:95], v[140:143], v[132:135], v[80:95]
	ds_read_b128 v[132:135], v209 offset:49152
	ds_read_b128 v[136:139], v209 offset:57344
	s_waitcnt lgkmcnt(1)
	v_mfma_f32_32x32x16_bf16 v[96:111], v[132:135], v[128:131], v[96:111]
	s_waitcnt lgkmcnt(0)
	v_mfma_f32_32x32x16_bf16 v[80:95], v[136:139], v[128:131], v[80:95]
	ds_read_b128 v[128:131], v208 offset:49152
	ds_read_b128 v[132:135], v208 offset:57344
	s_waitcnt lgkmcnt(1)
	v_mfma_f32_32x32x16_bf16 v[96:111], v[128:131], v[124:127], v[96:111]
	s_waitcnt lgkmcnt(0)
	v_mfma_f32_32x32x16_bf16 v[80:95], v[132:135], v[124:127], v[80:95]
	ds_read_b128 v[124:127], v213 offset:49152
	ds_read_b128 v[128:131], v213 offset:57344
	s_waitcnt lgkmcnt(1)
	v_mfma_f32_32x32x16_bf16 v[96:111], v[124:127], v[120:123], v[96:111]
	s_waitcnt lgkmcnt(0)
	v_mfma_f32_32x32x16_bf16 v[80:95], v[128:131], v[120:123], v[80:95]
	ds_read_b128 v[120:123], v214 offset:49152
	ds_read_b128 v[124:127], v214 offset:57344
	s_waitcnt lgkmcnt(1)
	v_mfma_f32_32x32x16_bf16 v[96:111], v[120:123], v[116:119], v[96:111]
	s_waitcnt lgkmcnt(0)
	v_mfma_f32_32x32x16_bf16 v[80:95], v[124:127], v[116:119], v[80:95]
	ds_read_b128 v[116:119], v215 offset:49152
	ds_read_b128 v[120:123], v215 offset:57344
	v_exp_f32_e32 v124, v78
	v_exp_f32_e32 v125, v79
	s_waitcnt lgkmcnt(1)
	v_mfma_f32_32x32x16_bf16 v[96:111], v[116:119], v[112:115], v[96:111]
	v_exp_f32_e32 v116, v70
	v_exp_f32_e32 v117, v71
	v_exp_f32_e32 v118, v72
	v_exp_f32_e32 v119, v73
	s_waitcnt lgkmcnt(0)
	v_mfma_f32_32x32x16_bf16 v[80:95], v[120:123], v[112:115], v[80:95]
	v_exp_f32_e32 v112, v64
	v_add_f32_e32 v64, 0, v231
	v_add_f32_e32 v64, v233, v64
	v_add_f32_e32 v64, v229, v64
	v_add_f32_e32 v64, v232, v64
	v_add_f32_e32 v64, v228, v64
	v_add_f32_e32 v64, v230, v64
	v_add_f32_e32 v64, v226, v64
	v_add_f32_e32 v64, v227, v64
	v_add_f32_e32 v64, v223, v64
	v_add_f32_e32 v64, v225, v64
	v_add_f32_e32 v64, v222, v64
	v_add_f32_e32 v64, v224, v64
	v_add_f32_e32 v64, v188, v64
	v_add_f32_e32 v64, v191, v64
	v_exp_f32_e32 v113, v66
	v_add_f32_e32 v64, v189, v64
	v_add_f32_e32 v64, v190, v64
	v_exp_f32_e32 v114, v68
	v_add_f32_e32 v64, v112, v64
	v_exp_f32_e32 v115, v69
	v_add_f32_e32 v64, v65, v64
	v_add_f32_e32 v64, v113, v64
	v_add_f32_e32 v64, v67, v64
	v_add_f32_e32 v64, v114, v64
	v_add_f32_e32 v64, v115, v64
	v_exp_f32_e32 v120, v74
	v_add_f32_e32 v64, v116, v64
	v_exp_f32_e32 v121, v75
	v_add_f32_e32 v64, v117, v64
	v_exp_f32_e32 v122, v76
	v_add_f32_e32 v64, v118, v64
	v_exp_f32_e32 v123, v77
	v_add_f32_e32 v64, v119, v64
	v_add_f32_e32 v64, v120, v64
	v_add_f32_e32 v64, v121, v64
	v_add_f32_e32 v64, v122, v64
	v_add_f32_e32 v64, v123, v64
	v_add_f32_e32 v64, v124, v64
	v_add_f32_e32 v64, v125, v64
	v_mov_b32_e32 v66, v64
	s_nop 1
	v_permlane32_swap_b32_e32 v64, v66
	v_cvt_pk_bf16_f32 v68, v231, v233
	v_cvt_pk_bf16_f32 v69, v229, v232
	v_cvt_pk_bf16_f32 v70, v228, v230
	v_cvt_pk_bf16_f32 v71, v226, v227
	v_cvt_pk_bf16_f32 v72, v223, v225
	v_cvt_pk_bf16_f32 v73, v222, v224
	v_cvt_pk_bf16_f32 v74, v188, v191
	v_cvt_pk_bf16_f32 v75, v189, v190
	v_cvt_pk_bf16_f32 v76, v112, v65
	v_cvt_pk_bf16_f32 v77, v113, v67
	v_cvt_pk_bf16_f32 v78, v114, v115
	v_cvt_pk_bf16_f32 v79, v116, v117
	v_cvt_pk_bf16_f32 v112, v118, v119
	v_cvt_pk_bf16_f32 v113, v120, v121
	v_cvt_pk_bf16_f32 v114, v122, v123
	v_cvt_pk_bf16_f32 v115, v124, v125
	s_nop 0
	v_permlane32_swap_b32_e32 v68, v70
	v_permlane32_swap_b32_e32 v69, v71
	v_permlane32_swap_b32_e32 v72, v74
	v_permlane32_swap_b32_e32 v73, v75
	v_permlane32_swap_b32_e32 v76, v78
	v_permlane32_swap_b32_e32 v77, v79
	v_permlane32_swap_b32_e32 v112, v114
	v_permlane32_swap_b32_e32 v113, v115
	ds_read_b64_tr_b16 v[116:117], v185 offset:0
	ds_read_b64_tr_b16 v[118:119], v185 offset:0x800
	ds_read_b64_tr_b16 v[120:121], v185 offset:0x1000
	ds_read_b64_tr_b16 v[122:123], v185 offset:0x1800
	ds_read_b64_tr_b16 v[124:125], v185 offset:0x2000
	ds_read_b64_tr_b16 v[126:127], v185 offset:0x2800
	ds_read_b64_tr_b16 v[128:129], v185 offset:0x3000
	ds_read_b64_tr_b16 v[130:131], v185 offset:0x3800
	s_waitcnt lgkmcnt(0)
	s_nop 0
	v_mfma_f32_32x32x16_bf16 v[0:15], v[68:71], v[116:119], v[0:15]
	ds_read_b64_tr_b16 v[116:117], v185 offset:0x200
	ds_read_b64_tr_b16 v[118:119], v185 offset:0xa00
	v_mfma_f32_32x32x16_bf16 v[0:15], v[72:75], v[120:123], v[0:15]
	ds_read_b64_tr_b16 v[120:121], v185 offset:0x1200
	ds_read_b64_tr_b16 v[122:123], v185 offset:0x1a00
	v_mfma_f32_32x32x16_bf16 v[0:15], v[76:79], v[124:127], v[0:15]
	ds_read_b64_tr_b16 v[124:125], v185 offset:0x2200
	ds_read_b64_tr_b16 v[126:127], v185 offset:0x2a00
	v_mfma_f32_32x32x16_bf16 v[0:15], v[112:115], v[128:131], v[0:15]
	ds_read_b64_tr_b16 v[128:129], v185 offset:0x3200
	ds_read_b64_tr_b16 v[130:131], v185 offset:0x3a00
	s_waitcnt lgkmcnt(0)
	v_mfma_f32_32x32x16_bf16 v[16:31], v[68:71], v[116:119], v[16:31]
	ds_read_b64_tr_b16 v[116:117], v185 offset:0x400
	ds_read_b64_tr_b16 v[118:119], v185 offset:0xc00
	v_mfma_f32_32x32x16_bf16 v[16:31], v[72:75], v[120:123], v[16:31]
	ds_read_b64_tr_b16 v[120:121], v185 offset:0x1400
	ds_read_b64_tr_b16 v[122:123], v185 offset:0x1c00
	v_mfma_f32_32x32x16_bf16 v[16:31], v[76:79], v[124:127], v[16:31]
	ds_read_b64_tr_b16 v[124:125], v185 offset:0x2400
	ds_read_b64_tr_b16 v[126:127], v185 offset:0x2c00
	v_mfma_f32_32x32x16_bf16 v[16:31], v[112:115], v[128:131], v[16:31]
	ds_read_b64_tr_b16 v[128:129], v185 offset:0x3400
	ds_read_b64_tr_b16 v[130:131], v185 offset:0x3c00
	s_waitcnt lgkmcnt(0)
	v_mfma_f32_32x32x16_bf16 v[32:47], v[68:71], v[116:119], v[32:47]
	ds_read_b64_tr_b16 v[116:117], v185 offset:0x600
	ds_read_b64_tr_b16 v[118:119], v185 offset:0xe00
	v_mfma_f32_32x32x16_bf16 v[32:47], v[72:75], v[120:123], v[32:47]
	ds_read_b64_tr_b16 v[120:121], v185 offset:0x1600
	ds_read_b64_tr_b16 v[122:123], v185 offset:0x1e00
	v_mfma_f32_32x32x16_bf16 v[32:47], v[76:79], v[124:127], v[32:47]
	ds_read_b64_tr_b16 v[124:125], v185 offset:0x2600
	ds_read_b64_tr_b16 v[126:127], v185 offset:0x2e00
	v_mfma_f32_32x32x16_bf16 v[32:47], v[112:115], v[128:131], v[32:47]
	ds_read_b64_tr_b16 v[128:129], v185 offset:0x3600
	ds_read_b64_tr_b16 v[130:131], v185 offset:0x3e00
	s_waitcnt lgkmcnt(0)
	v_mfma_f32_32x32x16_bf16 v[48:63], v[68:71], v[116:119], v[48:63]
	v_exp_f32_e32 v68, v96
	v_exp_f32_e32 v69, v97
	v_exp_f32_e32 v70, v98
	v_exp_f32_e32 v71, v99
	v_add_f32_e32 v65, 0, v68
	v_add_f32_e32 v65, v69, v65
	v_add_f32_e32 v65, v70, v65
	v_mfma_f32_32x32x16_bf16 v[48:63], v[72:75], v[120:123], v[48:63]
	v_exp_f32_e32 v72, v100
	v_exp_f32_e32 v73, v101
	v_exp_f32_e32 v74, v102
	v_exp_f32_e32 v75, v103
	v_add_f32_e32 v65, v71, v65
	v_add_f32_e32 v65, v72, v65
	v_add_f32_e32 v65, v73, v65
	v_mfma_f32_32x32x16_bf16 v[48:63], v[76:79], v[124:127], v[48:63]
	v_exp_f32_e32 v76, v104
	v_exp_f32_e32 v77, v105
	v_exp_f32_e32 v78, v106
	v_add_f32_e32 v65, v74, v65
	v_exp_f32_e32 v79, v107
	v_add_f32_e32 v65, v75, v65
	v_exp_f32_e32 v96, v108
	v_add_f32_e32 v65, v76, v65
	v_exp_f32_e32 v97, v109
	v_add_f32_e32 v65, v77, v65
	v_exp_f32_e32 v98, v110
	v_add_f32_e32 v65, v78, v65
	v_exp_f32_e32 v99, v111
	v_add_f32_e32 v65, v79, v65
	v_exp_f32_e32 v80, v80
	v_add_f32_e32 v65, v96, v65
	v_exp_f32_e32 v81, v81
	v_add_f32_e32 v65, v97, v65
	v_exp_f32_e32 v82, v82
	v_add_f32_e32 v65, v98, v65
	v_exp_f32_e32 v83, v83
	v_add_f32_e32 v65, v99, v65
	v_exp_f32_e32 v84, v84
	v_add_f32_e32 v65, v80, v65
	v_exp_f32_e32 v85, v85
	v_add_f32_e32 v65, v81, v65
	v_exp_f32_e32 v86, v86
	v_add_f32_e32 v65, v82, v65
	v_exp_f32_e32 v87, v87
	v_add_f32_e32 v65, v83, v65
	v_exp_f32_e32 v88, v88
	v_add_f32_e32 v65, v84, v65
	v_exp_f32_e32 v89, v89
	v_add_f32_e32 v65, v85, v65
	v_exp_f32_e32 v90, v90
	v_add_f32_e32 v65, v86, v65
	v_exp_f32_e32 v91, v91
	v_add_f32_e32 v65, v87, v65
	v_exp_f32_e32 v92, v92
	v_add_f32_e32 v65, v88, v65
	v_exp_f32_e32 v93, v93
	v_add_f32_e32 v65, v89, v65
	v_mfma_f32_32x32x16_bf16 v[48:63], v[112:115], v[128:131], v[48:63]
	v_exp_f32_e32 v94, v94
	v_add_f32_e32 v65, v90, v65
	v_exp_f32_e32 v95, v95
	v_add_f32_e32 v65, v91, v65
	v_add_f32_e32 v65, v92, v65
	v_add_f32_e32 v65, v93, v65
	v_add_f32_e32 v65, v94, v65
	v_add_f32_e32 v65, v95, v65
	v_mov_b32_e32 v67, v65
	s_barrier
	s_nop 0
	v_permlane32_swap_b32_e32 v65, v67
	v_cvt_pk_bf16_f32 v68, v68, v69
	v_cvt_pk_bf16_f32 v69, v70, v71
	v_cvt_pk_bf16_f32 v70, v72, v73
	v_cvt_pk_bf16_f32 v71, v74, v75
	v_cvt_pk_bf16_f32 v72, v76, v77
	v_cvt_pk_bf16_f32 v73, v78, v79
	v_cvt_pk_bf16_f32 v74, v96, v97
	v_cvt_pk_bf16_f32 v75, v98, v99
	v_cvt_pk_bf16_f32 v76, v80, v81
	v_cvt_pk_bf16_f32 v77, v82, v83
	v_cvt_pk_bf16_f32 v78, v84, v85
	v_cvt_pk_bf16_f32 v79, v86, v87
	v_cvt_pk_bf16_f32 v80, v88, v89
	v_cvt_pk_bf16_f32 v81, v90, v91
	v_cvt_pk_bf16_f32 v82, v92, v93
	v_cvt_pk_bf16_f32 v83, v94, v95
	s_nop 0
	v_permlane32_swap_b32_e32 v68, v70
	v_permlane32_swap_b32_e32 v69, v71
	v_permlane32_swap_b32_e32 v72, v74
	v_permlane32_swap_b32_e32 v73, v75
	v_permlane32_swap_b32_e32 v76, v78
	v_permlane32_swap_b32_e32 v77, v79
	v_permlane32_swap_b32_e32 v80, v82
	v_permlane32_swap_b32_e32 v81, v83
	ds_read_b64_tr_b16 v[84:85], v177 offset:0
	ds_read_b64_tr_b16 v[86:87], v177 offset:0x800
	ds_read_b64_tr_b16 v[88:89], v177 offset:0x1000
	ds_read_b64_tr_b16 v[90:91], v177 offset:0x1800
	ds_read_b64_tr_b16 v[92:93], v177 offset:0x2000
	ds_read_b64_tr_b16 v[94:95], v177 offset:0x2800
	ds_read_b64_tr_b16 v[96:97], v177 offset:0x3000
	ds_read_b64_tr_b16 v[98:99], v177 offset:0x3800
	s_waitcnt lgkmcnt(0)
	s_nop 0
	v_mfma_f32_32x32x16_bf16 v[0:15], v[68:71], v[84:87], v[0:15]
	ds_read_b64_tr_b16 v[84:85], v177 offset:0x200
	ds_read_b64_tr_b16 v[86:87], v177 offset:0xa00
	v_mfma_f32_32x32x16_bf16 v[0:15], v[72:75], v[88:91], v[0:15]
	ds_read_b64_tr_b16 v[88:89], v177 offset:0x1200
	ds_read_b64_tr_b16 v[90:91], v177 offset:0x1a00
	v_mfma_f32_32x32x16_bf16 v[0:15], v[76:79], v[92:95], v[0:15]
	ds_read_b64_tr_b16 v[92:93], v177 offset:0x2200
	ds_read_b64_tr_b16 v[94:95], v177 offset:0x2a00
	v_mfma_f32_32x32x16_bf16 v[0:15], v[80:83], v[96:99], v[0:15]
	ds_read_b64_tr_b16 v[96:97], v177 offset:0x3200
	ds_read_b64_tr_b16 v[98:99], v177 offset:0x3a00
	s_waitcnt lgkmcnt(0)
	v_mfma_f32_32x32x16_bf16 v[16:31], v[68:71], v[84:87], v[16:31]
	ds_read_b64_tr_b16 v[84:85], v177 offset:0x400
	ds_read_b64_tr_b16 v[86:87], v177 offset:0xc00
	v_mfma_f32_32x32x16_bf16 v[16:31], v[72:75], v[88:91], v[16:31]
	ds_read_b64_tr_b16 v[88:89], v177 offset:0x1400
	ds_read_b64_tr_b16 v[90:91], v177 offset:0x1c00
	v_mfma_f32_32x32x16_bf16 v[16:31], v[76:79], v[92:95], v[16:31]
	ds_read_b64_tr_b16 v[92:93], v177 offset:0x2400
	ds_read_b64_tr_b16 v[94:95], v177 offset:0x2c00
	v_mfma_f32_32x32x16_bf16 v[16:31], v[80:83], v[96:99], v[16:31]
	ds_read_b64_tr_b16 v[96:97], v177 offset:0x3400
	ds_read_b64_tr_b16 v[98:99], v177 offset:0x3c00
	s_waitcnt lgkmcnt(0)
	v_mfma_f32_32x32x16_bf16 v[32:47], v[68:71], v[84:87], v[32:47]
	ds_read_b64_tr_b16 v[84:85], v177 offset:0x600
	ds_read_b64_tr_b16 v[86:87], v177 offset:0xe00
	v_mfma_f32_32x32x16_bf16 v[32:47], v[72:75], v[88:91], v[32:47]
	ds_read_b64_tr_b16 v[88:89], v177 offset:0x1600
	ds_read_b64_tr_b16 v[90:91], v177 offset:0x1e00
	v_mfma_f32_32x32x16_bf16 v[32:47], v[76:79], v[92:95], v[32:47]
	ds_read_b64_tr_b16 v[92:93], v177 offset:0x2600
	ds_read_b64_tr_b16 v[94:95], v177 offset:0x2e00
	v_mfma_f32_32x32x16_bf16 v[32:47], v[80:83], v[96:99], v[32:47]
	ds_read_b64_tr_b16 v[96:97], v177 offset:0x3600
	ds_read_b64_tr_b16 v[98:99], v177 offset:0x3e00
	s_waitcnt lgkmcnt(0)
	v_mfma_f32_32x32x16_bf16 v[48:63], v[68:71], v[84:87], v[48:63]
	v_cmp_gt_u32_e32 vcc, 32, v202
	v_mfma_f32_32x32x16_bf16 v[48:63], v[72:75], v[88:91], v[48:63]
	v_mfma_f32_32x32x16_bf16 v[48:63], v[76:79], v[92:95], v[48:63]
	v_mfma_f32_32x32x16_bf16 v[48:63], v[80:83], v[96:99], v[48:63]
	s_and_saveexec_b64 s[2:3], vcc
	s_cbranch_execz .LBB0_582
	v_pk_add_f32 v[64:65], v[64:65], v[66:67]
	v_lshl_add_u32 v68, v200, 2, v144
	v_add_f32_e32 v64, v183, v64
	v_add_f32_e32 v64, v64, v65
	ds_write_b32 v68, v64
	s_branch .LBB0_582
